# speedup vs baseline: 1.6917x; 1.0027x over previous
.LBB1_36:
	s_or_b64 exec, exec, s[2:3]
	s_waitcnt vmcnt(0)
	v_add_f32_e32 v103, 0, v103
	v_add_f32_e32 v103, v103, v104
	v_add_f32_e32 v103, v103, v105
	v_add_f32_e32 v103, v103, v106
	v_add_f32_e32 v103, v103, v107
	v_add_f32_e32 v103, v103, v108
	v_add_f32_e32 v103, v103, v109
	v_add_f32_e32 v103, v103, v110
	v_add_f32_e32 v103, v103, v111
	v_add_f32_e32 v103, v103, v112
	v_add_f32_e32 v103, v103, v113
	v_add_f32_e32 v103, v103, v114
	v_add_f32_e32 v103, v103, v115
	v_add_f32_e32 v103, v103, v116
	v_add_f32_e32 v103, v103, v117
	v_add_f32_e32 v103, v103, v118
	v_add_f32_e32 v103, v103, v119
	v_add_f32_e32 v103, v103, v120
	v_add_f32_e32 v103, v103, v121
	v_add_f32_e32 v103, v103, v122
	s_mov_b32 s14, 0xf800000
	s_mov_b32 s11, 0x41e6d4ca
	v_cmp_gt_f32_e32 vcc, s14, v103
	v_mul_f32_e32 v104, 0x4f800000, v103
	s_nop 0
	v_cndmask_b32_e32 v104, v103, v104, vcc
	v_sqrt_f32_e32 v103, v104
	s_nop 0
	v_add_u32_e32 v105, -1, v103
	v_fma_f32 v108, -v105, v103, v104
	v_cmp_ge_f32_e64 s[2:3], 0, v108
	v_add_u32_e32 v108, 1, v103
	s_nop 0
	v_cndmask_b32_e64 v105, v103, v105, s[2:3]
	v_fma_f32 v103, -v108, v103, v104
	v_cmp_lt_f32_e64 s[2:3], 0, v103
	s_nop 1
	v_cndmask_b32_e64 v103, v105, v108, s[2:3]
	v_mul_f32_e32 v105, 0x37800000, v103
	v_cndmask_b32_e32 v105, v103, v105, vcc
	v_mov_b32_e32 v103, 0x260
	v_cmp_class_f32_e32 vcc, v104, v103
	s_nop 1
	v_cndmask_b32_e32 v104, v105, v104, vcc
	v_add_f32_e32 v104, 0x322bcc77, v104
	v_div_scale_f32 v108, s[2:3], v104, v104, s11
	v_rcp_f32_e32 v105, v108
	s_nop 0
	v_fma_f32 v109, -v108, v105, 1.0
	v_fmac_f32_e32 v105, v109, v105
	v_div_scale_f32 v107, vcc, s11, v104, s11
	v_mul_f32_e32 v106, v107, v105
	v_fma_f32 v111, -v108, v106, v107
	v_fmac_f32_e32 v106, v111, v105
	v_fma_f32 v107, -v108, v106, v107
	s_nop 0
	v_div_fmas_f32 v109, v107, v105, v106
	v_div_fixup_f32 v109, v109, v104, s11
	v_lshlrev_b32_e32 v110, 2, v101
	ds_bpermute_b32 v108, v110, v109
	ds_bpermute_b32 v111, v110, v109 offset:64
	ds_bpermute_b32 v112, v110, v109 offset:128
	ds_bpermute_b32 v113, v110, v109 offset:192
	s_mul_i32 s2, s23, 0x1f80
	s_add_i32 s6, s8, s2
	s_movk_i32 s2, 0x88
	v_and_b32_e32 v66, 0x70, v100
	v_add_u32_e32 v71, s10, v66
	v_lshrrev_b32_e32 v67, 4, v100
	v_lshlrev_b32_e32 v67, 3, v67
	v_add_u32_e32 v72, s6, v67
	s_mov_b32 s34, 0x3d0df4e0
	v_mad_u32_u24 v120, v101, s2, v72
	ds_read_b128 v[114:117], v71 offset:8832
	s_waitcnt lgkmcnt(0)
	v_mul_f32_e32 v64, v114, v108
	v_mul_f32_e32 v65, v115, v108
	v_mul_f32_e32 v66, v116, v108
	v_mul_f32_e32 v67, v117, v108
	v_fmaak_f32 v60, v60, v64, 0xc1e6d4ca
	v_fmaak_f32 v61, v61, v65, 0xc1e6d4ca
	v_fmaak_f32 v62, v62, v66, 0xc1e6d4ca
	v_fmaak_f32 v63, v63, v67, 0xc1e6d4ca
	v_exp_f32_e32 v64, v60
	v_exp_f32_e32 v65, v61
	v_exp_f32_e32 v66, v62
	v_exp_f32_e32 v67, v63
	v_fma_f32 v60, v60, s34, 1.0
	v_fma_f32 v61, v61, s34, 1.0
	v_fma_f32 v62, v62, s34, 1.0
	v_fma_f32 v63, v63, s34, 1.0
	v_mul_f32_e32 v60, v64, v60
	v_mul_f32_e32 v61, v65, v61
	v_mul_f32_e32 v62, v66, v62
	v_mul_f32_e32 v63, v67, v63
	v_cvt_pk_bf16_f32 v68, v64, v65
	v_cvt_pk_bf16_f32 v69, v66, v67
	ds_write_b64 v120, v[68:69] offset:10240
	v_cvt_pk_bf16_f32 v72, v60, v61
	v_cvt_pk_bf16_f32 v73, v62, v63
	v_mul_f32_e32 v64, v114, v111
	v_mul_f32_e32 v65, v115, v111
	v_mul_f32_e32 v66, v116, v111
	v_mul_f32_e32 v67, v117, v111
	v_fmaak_f32 v56, v56, v64, 0xc1e6d4ca
	v_fmaak_f32 v57, v57, v65, 0xc1e6d4ca
	v_fmaak_f32 v58, v58, v66, 0xc1e6d4ca
	v_fmaak_f32 v59, v59, v67, 0xc1e6d4ca
	v_exp_f32_e32 v64, v56
	v_exp_f32_e32 v65, v57
	v_exp_f32_e32 v66, v58
	v_exp_f32_e32 v67, v59
	v_fma_f32 v56, v56, s34, 1.0
	v_fma_f32 v57, v57, s34, 1.0
	v_fma_f32 v58, v58, s34, 1.0
	v_fma_f32 v59, v59, s34, 1.0
	v_mul_f32_e32 v56, v64, v56
	v_mul_f32_e32 v57, v65, v57
	v_mul_f32_e32 v58, v66, v58
	v_mul_f32_e32 v59, v67, v59
	v_cvt_pk_bf16_f32 v68, v64, v65
	v_cvt_pk_bf16_f32 v69, v66, v67
	ds_write_b64 v120, v[68:69] offset:12416
	v_cvt_pk_bf16_f32 v74, v56, v57
	v_cvt_pk_bf16_f32 v75, v58, v59
	v_mul_f32_e32 v64, v114, v112
	v_mul_f32_e32 v65, v115, v112
	v_mul_f32_e32 v66, v116, v112
	v_mul_f32_e32 v67, v117, v112
	v_fmaak_f32 v52, v52, v64, 0xc1e6d4ca
	v_fmaak_f32 v53, v53, v65, 0xc1e6d4ca
	v_fmaak_f32 v54, v54, v66, 0xc1e6d4ca
	v_fmaak_f32 v55, v55, v67, 0xc1e6d4ca
	v_exp_f32_e32 v64, v52
	v_exp_f32_e32 v65, v53
	v_exp_f32_e32 v66, v54
	v_exp_f32_e32 v67, v55
	v_fma_f32 v52, v52, s34, 1.0
	v_fma_f32 v53, v53, s34, 1.0
	v_fma_f32 v54, v54, s34, 1.0
	v_fma_f32 v55, v55, s34, 1.0
	v_mul_f32_e32 v52, v64, v52
	v_mul_f32_e32 v53, v65, v53
	v_mul_f32_e32 v54, v66, v54
	v_mul_f32_e32 v55, v67, v55
	v_cvt_pk_bf16_f32 v68, v64, v65
	v_cvt_pk_bf16_f32 v69, v66, v67
	ds_write_b64 v120, v[68:69] offset:14592
	v_cvt_pk_bf16_f32 v76, v52, v53
	v_cvt_pk_bf16_f32 v77, v54, v55
	v_mul_f32_e32 v64, v114, v113
	v_mul_f32_e32 v65, v115, v113
	v_mul_f32_e32 v66, v116, v113
	v_mul_f32_e32 v67, v117, v113
	ds_read_b128 v[114:117], v71 offset:8896
	v_fmaak_f32 v48, v48, v64, 0xc1e6d4ca
	v_fmaak_f32 v49, v49, v65, 0xc1e6d4ca
	v_fmaak_f32 v50, v50, v66, 0xc1e6d4ca
	v_fmaak_f32 v51, v51, v67, 0xc1e6d4ca
	v_exp_f32_e32 v64, v48
	v_exp_f32_e32 v65, v49
	v_exp_f32_e32 v66, v50
	v_exp_f32_e32 v67, v51
	v_fma_f32 v48, v48, s34, 1.0
	v_fma_f32 v49, v49, s34, 1.0
	v_fma_f32 v50, v50, s34, 1.0
	v_fma_f32 v51, v51, s34, 1.0
	v_mul_f32_e32 v48, v64, v48
	v_mul_f32_e32 v49, v65, v49
	v_mul_f32_e32 v50, v66, v50
	v_mul_f32_e32 v51, v67, v51
	v_cvt_pk_bf16_f32 v68, v64, v65
	v_cvt_pk_bf16_f32 v69, v66, v67
	ds_write_b64 v120, v[68:69] offset:16768
	v_cvt_pk_bf16_f32 v78, v48, v49
	v_cvt_pk_bf16_f32 v79, v50, v51
	s_waitcnt lgkmcnt(0)
	v_mul_f32_e32 v64, v114, v108
	v_mul_f32_e32 v65, v115, v108
	v_mul_f32_e32 v66, v116, v108
	v_mul_f32_e32 v67, v117, v108
	v_fmaak_f32 v44, v44, v64, 0xc1e6d4ca
	v_fmaak_f32 v45, v45, v65, 0xc1e6d4ca
	v_fmaak_f32 v46, v46, v66, 0xc1e6d4ca
	v_fmaak_f32 v47, v47, v67, 0xc1e6d4ca
	v_exp_f32_e32 v64, v44
	v_exp_f32_e32 v65, v45
	v_exp_f32_e32 v66, v46
	v_exp_f32_e32 v67, v47
	v_fma_f32 v44, v44, s34, 1.0
	v_fma_f32 v45, v45, s34, 1.0
	v_fma_f32 v46, v46, s34, 1.0
	v_fma_f32 v47, v47, s34, 1.0
	v_mul_f32_e32 v44, v64, v44
	v_mul_f32_e32 v45, v65, v45
	v_mul_f32_e32 v46, v66, v46
	v_mul_f32_e32 v47, v67, v47
	v_cvt_pk_bf16_f32 v68, v64, v65
	v_cvt_pk_bf16_f32 v69, v66, v67
	ds_write_b64 v120, v[68:69] offset:10272
	v_cvt_pk_bf16_f32 v80, v44, v45
	v_cvt_pk_bf16_f32 v81, v46, v47
	v_mul_f32_e32 v64, v114, v111
	v_mul_f32_e32 v65, v115, v111
	v_mul_f32_e32 v66, v116, v111
	v_mul_f32_e32 v67, v117, v111
	v_fmaak_f32 v40, v40, v64, 0xc1e6d4ca
	v_fmaak_f32 v41, v41, v65, 0xc1e6d4ca
	v_fmaak_f32 v42, v42, v66, 0xc1e6d4ca
	v_fmaak_f32 v43, v43, v67, 0xc1e6d4ca
	v_exp_f32_e32 v64, v40
	v_exp_f32_e32 v65, v41
	v_exp_f32_e32 v66, v42
	v_exp_f32_e32 v67, v43
	v_fma_f32 v40, v40, s34, 1.0
	v_fma_f32 v41, v41, s34, 1.0
	v_fma_f32 v42, v42, s34, 1.0
	v_fma_f32 v43, v43, s34, 1.0
	v_mul_f32_e32 v40, v64, v40
	v_mul_f32_e32 v41, v65, v41
	v_mul_f32_e32 v42, v66, v42
	v_mul_f32_e32 v43, v67, v43
	v_cvt_pk_bf16_f32 v68, v64, v65
	v_cvt_pk_bf16_f32 v69, v66, v67
	ds_write_b64 v120, v[68:69] offset:12448
	v_cvt_pk_bf16_f32 v82, v40, v41
	v_cvt_pk_bf16_f32 v83, v42, v43
	v_mul_f32_e32 v64, v114, v112
	v_mul_f32_e32 v65, v115, v112
	v_mul_f32_e32 v66, v116, v112
	v_mul_f32_e32 v67, v117, v112
	v_fmaak_f32 v36, v36, v64, 0xc1e6d4ca
	v_fmaak_f32 v37, v37, v65, 0xc1e6d4ca
	v_fmaak_f32 v38, v38, v66, 0xc1e6d4ca
	v_fmaak_f32 v39, v39, v67, 0xc1e6d4ca
	v_exp_f32_e32 v64, v36
	v_exp_f32_e32 v65, v37
	v_exp_f32_e32 v66, v38
	v_exp_f32_e32 v67, v39
	v_fma_f32 v36, v36, s34, 1.0
	v_fma_f32 v37, v37, s34, 1.0
	v_fma_f32 v38, v38, s34, 1.0
	v_fma_f32 v39, v39, s34, 1.0
	v_mul_f32_e32 v36, v64, v36
	v_mul_f32_e32 v37, v65, v37
	v_mul_f32_e32 v38, v66, v38
	v_mul_f32_e32 v39, v67, v39
	v_cvt_pk_bf16_f32 v68, v64, v65
	v_cvt_pk_bf16_f32 v69, v66, v67
	ds_write_b64 v120, v[68:69] offset:14624
	v_cvt_pk_bf16_f32 v84, v36, v37
	v_cvt_pk_bf16_f32 v85, v38, v39
	v_mul_f32_e32 v64, v114, v113
	v_mul_f32_e32 v65, v115, v113
	v_mul_f32_e32 v66, v116, v113
	v_mul_f32_e32 v67, v117, v113
	ds_read_b128 v[114:117], v71 offset:8960
	v_fmaak_f32 v32, v32, v64, 0xc1e6d4ca
	v_fmaak_f32 v33, v33, v65, 0xc1e6d4ca
	v_fmaak_f32 v34, v34, v66, 0xc1e6d4ca
	v_fmaak_f32 v35, v35, v67, 0xc1e6d4ca
	v_exp_f32_e32 v64, v32
	v_exp_f32_e32 v65, v33
	v_exp_f32_e32 v66, v34
	v_exp_f32_e32 v67, v35
	v_fma_f32 v32, v32, s34, 1.0
	v_fma_f32 v33, v33, s34, 1.0
	v_fma_f32 v34, v34, s34, 1.0
	v_fma_f32 v35, v35, s34, 1.0
	v_mul_f32_e32 v32, v64, v32
	v_mul_f32_e32 v33, v65, v33
	v_mul_f32_e32 v34, v66, v34
	v_mul_f32_e32 v35, v67, v35
	v_cvt_pk_bf16_f32 v68, v64, v65
	v_cvt_pk_bf16_f32 v69, v66, v67
	ds_write_b64 v120, v[68:69] offset:16800
	v_cvt_pk_bf16_f32 v86, v32, v33
	v_cvt_pk_bf16_f32 v87, v34, v35
	s_waitcnt lgkmcnt(0)
	v_mul_f32_e32 v64, v114, v108
	v_mul_f32_e32 v65, v115, v108
	v_mul_f32_e32 v66, v116, v108
	v_mul_f32_e32 v67, v117, v108
	v_fmaak_f32 v28, v28, v64, 0xc1e6d4ca
	v_fmaak_f32 v29, v29, v65, 0xc1e6d4ca
	v_fmaak_f32 v30, v30, v66, 0xc1e6d4ca
	v_fmaak_f32 v31, v31, v67, 0xc1e6d4ca
	v_exp_f32_e32 v64, v28
	v_exp_f32_e32 v65, v29
	v_exp_f32_e32 v66, v30
	v_exp_f32_e32 v67, v31
	v_fma_f32 v28, v28, s34, 1.0
	v_fma_f32 v29, v29, s34, 1.0
	v_fma_f32 v30, v30, s34, 1.0
	v_fma_f32 v31, v31, s34, 1.0
	v_mul_f32_e32 v28, v64, v28
	v_mul_f32_e32 v29, v65, v29
	v_mul_f32_e32 v30, v66, v30
	v_mul_f32_e32 v31, v67, v31
	v_cvt_pk_bf16_f32 v68, v64, v65
	v_cvt_pk_bf16_f32 v69, v66, v67
	ds_write_b64 v120, v[68:69] offset:10304
	v_cvt_pk_bf16_f32 v88, v28, v29
	v_cvt_pk_bf16_f32 v89, v30, v31
	v_mul_f32_e32 v64, v114, v111
	v_mul_f32_e32 v65, v115, v111
	v_mul_f32_e32 v66, v116, v111
	v_mul_f32_e32 v67, v117, v111
	v_fmaak_f32 v24, v24, v64, 0xc1e6d4ca
	v_fmaak_f32 v25, v25, v65, 0xc1e6d4ca
	v_fmaak_f32 v26, v26, v66, 0xc1e6d4ca
	v_fmaak_f32 v27, v27, v67, 0xc1e6d4ca
	v_exp_f32_e32 v64, v24
	v_exp_f32_e32 v65, v25
	v_exp_f32_e32 v66, v26
	v_exp_f32_e32 v67, v27
	v_fma_f32 v24, v24, s34, 1.0
	v_fma_f32 v25, v25, s34, 1.0
	v_fma_f32 v26, v26, s34, 1.0
	v_fma_f32 v27, v27, s34, 1.0
	v_mul_f32_e32 v24, v64, v24
	v_mul_f32_e32 v25, v65, v25
	v_mul_f32_e32 v26, v66, v26
	v_mul_f32_e32 v27, v67, v27
	v_cvt_pk_bf16_f32 v68, v64, v65
	v_cvt_pk_bf16_f32 v69, v66, v67
	ds_write_b64 v120, v[68:69] offset:12480
	v_cvt_pk_bf16_f32 v90, v24, v25
	v_cvt_pk_bf16_f32 v91, v26, v27
	v_mul_f32_e32 v64, v114, v112
	v_mul_f32_e32 v65, v115, v112
	v_mul_f32_e32 v66, v116, v112
	v_mul_f32_e32 v67, v117, v112
	v_fmaak_f32 v20, v20, v64, 0xc1e6d4ca
	v_fmaak_f32 v21, v21, v65, 0xc1e6d4ca
	v_fmaak_f32 v22, v22, v66, 0xc1e6d4ca
	v_fmaak_f32 v23, v23, v67, 0xc1e6d4ca
	v_exp_f32_e32 v64, v20
	v_exp_f32_e32 v65, v21
	v_exp_f32_e32 v66, v22
	v_exp_f32_e32 v67, v23
	v_fma_f32 v20, v20, s34, 1.0
	v_fma_f32 v21, v21, s34, 1.0
	v_fma_f32 v22, v22, s34, 1.0
	v_fma_f32 v23, v23, s34, 1.0
	v_mul_f32_e32 v20, v64, v20
	v_mul_f32_e32 v21, v65, v21
	v_mul_f32_e32 v22, v66, v22
	v_mul_f32_e32 v23, v67, v23
	v_cvt_pk_bf16_f32 v68, v64, v65
	v_cvt_pk_bf16_f32 v69, v66, v67
	ds_write_b64 v120, v[68:69] offset:14656
	v_cvt_pk_bf16_f32 v92, v20, v21
	v_cvt_pk_bf16_f32 v93, v22, v23
	v_mul_f32_e32 v64, v114, v113
	v_mul_f32_e32 v65, v115, v113
	v_mul_f32_e32 v66, v116, v113
	v_mul_f32_e32 v67, v117, v113
	ds_read_b128 v[114:117], v71 offset:9024
	v_fmaak_f32 v16, v16, v64, 0xc1e6d4ca
	v_fmaak_f32 v17, v17, v65, 0xc1e6d4ca
	v_fmaak_f32 v18, v18, v66, 0xc1e6d4ca
	v_fmaak_f32 v19, v19, v67, 0xc1e6d4ca
	v_exp_f32_e32 v64, v16
	v_exp_f32_e32 v65, v17
	v_exp_f32_e32 v66, v18
	v_exp_f32_e32 v67, v19
	v_fma_f32 v16, v16, s34, 1.0
	v_fma_f32 v17, v17, s34, 1.0
	v_fma_f32 v18, v18, s34, 1.0
	v_fma_f32 v19, v19, s34, 1.0
	v_mul_f32_e32 v16, v64, v16
	v_mul_f32_e32 v17, v65, v17
	v_mul_f32_e32 v18, v66, v18
	v_mul_f32_e32 v19, v67, v19
	v_cvt_pk_bf16_f32 v68, v64, v65
	v_cvt_pk_bf16_f32 v69, v66, v67
	ds_write_b64 v120, v[68:69] offset:16832
	v_cvt_pk_bf16_f32 v94, v16, v17
	v_cvt_pk_bf16_f32 v95, v18, v19
	s_waitcnt lgkmcnt(0)
	v_mul_f32_e32 v64, v114, v108
	v_mul_f32_e32 v65, v115, v108
	v_mul_f32_e32 v66, v116, v108
	v_mul_f32_e32 v67, v117, v108
	v_fmaak_f32 v12, v12, v64, 0xc1e6d4ca
	v_fmaak_f32 v13, v13, v65, 0xc1e6d4ca
	v_fmaak_f32 v14, v14, v66, 0xc1e6d4ca
	v_fmaak_f32 v15, v15, v67, 0xc1e6d4ca
	v_exp_f32_e32 v64, v12
	v_exp_f32_e32 v65, v13
	v_exp_f32_e32 v66, v14
	v_exp_f32_e32 v67, v15
	v_fma_f32 v12, v12, s34, 1.0
	v_fma_f32 v13, v13, s34, 1.0
	v_fma_f32 v14, v14, s34, 1.0
	v_fma_f32 v15, v15, s34, 1.0
	v_mul_f32_e32 v12, v64, v12
	v_mul_f32_e32 v13, v65, v13
	v_mul_f32_e32 v14, v66, v14
	v_mul_f32_e32 v15, v67, v15
	v_cvt_pk_bf16_f32 v68, v64, v65
	v_cvt_pk_bf16_f32 v69, v66, v67
	ds_write_b64 v120, v[68:69] offset:10336
	v_cvt_pk_bf16_f32 v96, v12, v13
	v_cvt_pk_bf16_f32 v97, v14, v15
	v_mul_f32_e32 v64, v114, v111
	v_mul_f32_e32 v65, v115, v111
	v_mul_f32_e32 v66, v116, v111
	v_mul_f32_e32 v67, v117, v111
	v_fmaak_f32 v8, v8, v64, 0xc1e6d4ca
	v_fmaak_f32 v9, v9, v65, 0xc1e6d4ca
	v_fmaak_f32 v10, v10, v66, 0xc1e6d4ca
	v_fmaak_f32 v11, v11, v67, 0xc1e6d4ca
	v_exp_f32_e32 v64, v8
	v_exp_f32_e32 v65, v9
	v_exp_f32_e32 v66, v10
	v_exp_f32_e32 v67, v11
	v_fma_f32 v8, v8, s34, 1.0
	v_fma_f32 v9, v9, s34, 1.0
	v_fma_f32 v10, v10, s34, 1.0
	v_fma_f32 v11, v11, s34, 1.0
	v_mul_f32_e32 v8, v64, v8
	v_mul_f32_e32 v9, v65, v9
	v_mul_f32_e32 v10, v66, v10
	v_mul_f32_e32 v11, v67, v11
	v_cvt_pk_bf16_f32 v68, v64, v65
	v_cvt_pk_bf16_f32 v69, v66, v67
	ds_write_b64 v120, v[68:69] offset:12512
	v_cvt_pk_bf16_f32 v98, v8, v9
	v_cvt_pk_bf16_f32 v99, v10, v11
	v_mul_f32_e32 v64, v114, v112
	v_mul_f32_e32 v65, v115, v112
	v_mul_f32_e32 v66, v116, v112
	v_mul_f32_e32 v67, v117, v112
	v_fmaak_f32 v4, v4, v64, 0xc1e6d4ca
	v_fmaak_f32 v5, v5, v65, 0xc1e6d4ca
	v_fmaak_f32 v6, v6, v66, 0xc1e6d4ca
	v_fmaak_f32 v7, v7, v67, 0xc1e6d4ca
	v_exp_f32_e32 v64, v4
	v_exp_f32_e32 v65, v5
	v_exp_f32_e32 v66, v6
	v_exp_f32_e32 v67, v7
	v_fma_f32 v4, v4, s34, 1.0
	v_fma_f32 v5, v5, s34, 1.0
	v_fma_f32 v6, v6, s34, 1.0
	v_fma_f32 v7, v7, s34, 1.0
	v_mul_f32_e32 v4, v64, v4
	v_mul_f32_e32 v5, v65, v5
	v_mul_f32_e32 v6, v66, v6
	v_mul_f32_e32 v7, v67, v7
	v_cvt_pk_bf16_f32 v68, v64, v65
	v_cvt_pk_bf16_f32 v69, v66, v67
	ds_write_b64 v120, v[68:69] offset:14688
	v_cvt_pk_bf16_f32 v104, v4, v5
	v_cvt_pk_bf16_f32 v105, v6, v7
	v_mul_f32_e32 v64, v114, v113
	v_mul_f32_e32 v65, v115, v113
	v_mul_f32_e32 v66, v116, v113
	v_mul_f32_e32 v67, v117, v113
	v_fmaak_f32 v0, v0, v64, 0xc1e6d4ca
	v_fmaak_f32 v1, v1, v65, 0xc1e6d4ca
	v_fmaak_f32 v2, v2, v66, 0xc1e6d4ca
	v_fmaak_f32 v3, v3, v67, 0xc1e6d4ca
	v_exp_f32_e32 v64, v0
	v_exp_f32_e32 v65, v1
	v_exp_f32_e32 v66, v2
	v_exp_f32_e32 v67, v3
	v_fma_f32 v0, v0, s34, 1.0
	v_fma_f32 v1, v1, s34, 1.0
	v_fma_f32 v2, v2, s34, 1.0
	v_fma_f32 v3, v3, s34, 1.0
	v_mul_f32_e32 v0, v64, v0
	v_mul_f32_e32 v1, v65, v1
	v_mul_f32_e32 v2, v66, v2
	v_mul_f32_e32 v3, v67, v3
	v_cvt_pk_bf16_f32 v68, v64, v65
	v_cvt_pk_bf16_f32 v69, v66, v67
	ds_write_b64 v120, v[68:69] offset:16864
	v_cvt_pk_bf16_f32 v106, v0, v1
	v_cvt_pk_bf16_f32 v107, v2, v3
	s_movk_i32 s34, 0x88
	v_and_b32_e32 v64, 32, v100
	v_and_b32_e32 v66, 16, v100
	v_mad_u32_u24 v65, v101, s34, v64
	v_add_u32_e32 v65, s6, v65
	v_add_u32_e32 v67, v65, v66
	v_sub_u32_e32 v65, v65, v66
	v_lshrrev_b32_e32 v68, 1, v100
	v_and_b32_e32 v68, 16, v68
	v_bfe_u32 v69, v100, 2, 2
	v_or_b32_e32 v68, v68, v69
	v_and_b32_e32 v69, 3, v100
	v_lshlrev_b32_e32 v69, 3, v69
	v_mad_u32_u24 v68, v68, s34, v69
	v_add_u32_e32 v68, s6, v68
	s_movk_i32 s35, 0x44
	v_mul_u32_u24_e32 v66, s35, v66
	v_add_u32_e32 v69, v68, v66
	v_sub_u32_e32 v68, v68, v66
	ds_read_b64 v[0:1], v67 offset:10240
	ds_read_b64 v[2:3], v65 offset:10264
	ds_read_b64 v[4:5], v67 offset:10304
	ds_read_b64 v[6:7], v65 offset:10328
	ds_read_b64 v[8:9], v67 offset:12424
	ds_read_b64 v[10:11], v67 offset:12416
	ds_read_b64 v[12:13], v67 offset:12488
	ds_read_b64 v[14:15], v67 offset:12480
	ds_read_b64 v[16:17], v65 offset:14608
	ds_read_b64 v[18:19], v67 offset:14600
	ds_read_b64 v[20:21], v65 offset:14672
	ds_read_b64 v[22:23], v67 offset:14664
	ds_read_b64 v[24:25], v65 offset:16792
	ds_read_b64 v[26:27], v65 offset:16784
	ds_read_b64 v[28:29], v65 offset:16856
	ds_read_b64 v[30:31], v65 offset:16848
	ds_read_b64_tr_b16 v[32:33], v69 offset:10240
	ds_read_b64_tr_b16 v[34:35], v68 offset:11872
	ds_read_b64_tr_b16 v[36:37], v69 offset:14592
	ds_read_b64_tr_b16 v[38:39], v68 offset:16224
	ds_read_b64_tr_b16 v[40:41], v69 offset:10816
	ds_read_b64_tr_b16 v[42:43], v69 offset:10272
	ds_read_b64_tr_b16 v[44:45], v69 offset:15168
	ds_read_b64_tr_b16 v[46:47], v69 offset:14624
	ds_read_b64_tr_b16 v[48:49], v68 offset:11392
	ds_read_b64_tr_b16 v[50:51], v69 offset:10848
	ds_read_b64_tr_b16 v[52:53], v68 offset:15744
	ds_read_b64_tr_b16 v[54:55], v69 offset:15200
	ds_read_b64_tr_b16 v[56:57], v68 offset:11968
	ds_read_b64_tr_b16 v[58:59], v68 offset:11424
	ds_read_b64_tr_b16 v[60:61], v68 offset:16320
	ds_read_b64_tr_b16 v[62:63], v68 offset:15776
	ds_read2st64_b32 v[116:117], v102 offset0:22 offset1:23
	s_waitcnt lgkmcnt(0)
	ds_write_b64 v120, v[72:73] offset:10240
	ds_write_b64 v120, v[74:75] offset:12416
	ds_write_b64 v120, v[76:77] offset:14592
	ds_write_b64 v120, v[78:79] offset:16768
	ds_write_b64 v120, v[80:81] offset:10272
	ds_write_b64 v120, v[82:83] offset:12448
	ds_write_b64 v120, v[84:85] offset:14624
	ds_write_b64 v120, v[86:87] offset:16800
	ds_write_b64 v120, v[88:89] offset:10304
	ds_write_b64 v120, v[90:91] offset:12480
	ds_write_b64 v120, v[92:93] offset:14656
	ds_write_b64 v120, v[94:95] offset:16832
	ds_write_b64 v120, v[96:97] offset:10336
	ds_write_b64 v120, v[98:99] offset:12512
	ds_write_b64 v120, v[104:105] offset:14688
	ds_write_b64 v120, v[106:107] offset:16864
	v_and_b32_e32 v110, 1, v100
	v_cmp_eq_u32_e32 vcc, 0, v110
	v_mov_b32_e32 v110, 0xeeeeeeee
	v_mov_b32_e32 v111, 0x44444444
	s_mov_b32 s32, 0x2b8cbccc
	s_mov_b32 s33, 0
	v_cndmask_b32_e32 v64, v110, v111, vcc
	v_mov_b32_e32 v68, 0x3f803f80
	v_mov_b32_e32 v69, v68
	v_mov_b32_e32 v70, v68
	v_mov_b32_e32 v71, v68
	v_mov_b64_e32 v[72:73], s[32:33]
	v_mov_b64_e32 v[76:77], s[32:33]
	v_mov_b64_e32 v[80:81], s[32:33]
	v_mov_b64_e32 v[84:85], s[32:33]
	v_mov_b64_e32 v[88:89], s[32:33]
	v_mov_b64_e32 v[92:93], s[32:33]
	v_mov_b64_e32 v[96:97], s[32:33]
	v_mov_b64_e32 v[104:105], s[32:33]
	s_movk_i32 s30, 100
	v_mov_b32_e32 v122, 0
	s_waitcnt lgkmcnt(0)
	v_mov_b32_dpp v112, v116 quad_perm:[0,2,0,2] row_mask:0xf bank_mask:0xf
	v_mov_b32_dpp v113, v116 quad_perm:[1,3,1,3] row_mask:0xf bank_mask:0xf
	v_mov_b32_dpp v114, v117 quad_perm:[0,2,0,2] row_mask:0xf bank_mask:0xf
	v_mov_b32_dpp v115, v117 quad_perm:[1,3,1,3] row_mask:0xf bank_mask:0xf
	v_smfmac_f32_16x16x64_bf16 v[72:75], v[68:71], v[0:7], v64
	v_smfmac_f32_16x16x64_bf16 v[76:79], v[68:71], v[8:15], v64
	v_smfmac_f32_16x16x64_bf16 v[80:83], v[68:71], v[16:23], v64
	v_smfmac_f32_16x16x64_bf16 v[84:87], v[68:71], v[24:31], v64
	s_nop 0
.Lsk_loop:
	s_nop 3
	v_add_f32_dpp v108, v72, v73 quad_perm:[0,1,2,3] row_mask:0x1 bank_mask:0xf
	v_add_f32_dpp v108, v76, v77 quad_perm:[0,1,2,3] row_mask:0x2 bank_mask:0xf
	v_add_f32_dpp v108, v80, v81 quad_perm:[0,1,2,3] row_mask:0x4 bank_mask:0xf
	v_add_f32_dpp v108, v84, v85 quad_perm:[0,1,2,3] row_mask:0x8 bank_mask:0xf
	v_rcp_f32_e32 v109, v108
	v_mov_b64_e32 v[88:89], s[32:33]
	v_mov_b64_e32 v[92:93], s[32:33]
	v_mul_f32_dpp v110, v109, v114 quad_perm:[0,2,0,2] row_mask:0xf bank_mask:0xf
	v_mul_f32_dpp v111, v109, v115 quad_perm:[1,3,1,3] row_mask:0xf bank_mask:0xf
	v_cvt_pk_bf16_f32 v68, v110, v111
	v_mov_b64_e32 v[96:97], s[32:33]
	v_mov_b64_e32 v[104:105], s[32:33]
	v_mov_b32_dpp v69, v68 row_ror:4 row_mask:0xf bank_mask:0xf
	v_mov_b32_dpp v70, v68 row_ror:8 row_mask:0xf bank_mask:0xf
	v_mov_b32_dpp v71, v68 row_ror:12 row_mask:0xf bank_mask:0xf
	s_nop 1
	v_smfmac_f32_16x16x64_bf16 v[88:91], v[68:71], v[32:39], v64
	v_smfmac_f32_16x16x64_bf16 v[92:95], v[68:71], v[40:47], v64
	v_smfmac_f32_16x16x64_bf16 v[96:99], v[68:71], v[48:55], v64
	v_smfmac_f32_16x16x64_bf16 v[104:107], v[68:71], v[56:63], v64
	s_nop 4
	v_add_f32_dpp v108, v88, v89 quad_perm:[0,1,2,3] row_mask:0x1 bank_mask:0xf
	v_add_f32_dpp v108, v92, v93 quad_perm:[0,1,2,3] row_mask:0x2 bank_mask:0xf
	v_add_f32_dpp v108, v96, v97 quad_perm:[0,1,2,3] row_mask:0x4 bank_mask:0xf
	v_add_f32_dpp v108, v104, v105 quad_perm:[0,1,2,3] row_mask:0x8 bank_mask:0xf
	v_rcp_f32_e32 v109, v108
	v_mov_b64_e32 v[72:73], s[32:33]
	v_mov_b64_e32 v[76:77], s[32:33]
	v_mul_f32_dpp v110, v109, v112 quad_perm:[0,2,0,2] row_mask:0xf bank_mask:0xf
	v_mul_f32_dpp v111, v109, v113 quad_perm:[1,3,1,3] row_mask:0xf bank_mask:0xf
	v_cvt_pk_bf16_f32 v68, v110, v111
	v_mov_b64_e32 v[80:81], s[32:33]
	v_mov_b64_e32 v[84:85], s[32:33]
	v_mov_b32_dpp v69, v68 row_ror:4 row_mask:0xf bank_mask:0xf
	v_mov_b32_dpp v70, v68 row_ror:8 row_mask:0xf bank_mask:0xf
	v_mov_b32_dpp v71, v68 row_ror:12 row_mask:0xf bank_mask:0xf
	v_cmp_ne_u32_e32 vcc, v68, v122
	v_mov_b32_e32 v122, v68
	s_cmp_eq_u64 vcc, 0
	s_cselect_b32 s30, 1, s30
	s_add_i32 s30, s30, -1
	s_cmp_lg_u32 s30, 0
	v_smfmac_f32_16x16x64_bf16 v[72:75], v[68:71], v[0:7], v64
	v_smfmac_f32_16x16x64_bf16 v[76:79], v[68:71], v[8:15], v64
	v_smfmac_f32_16x16x64_bf16 v[80:83], v[68:71], v[16:23], v64
	v_smfmac_f32_16x16x64_bf16 v[84:87], v[68:71], v[24:31], v64
	s_cbranch_scc1 .Lsk_loop
	s_nop 3
	v_add_f32_dpp v108, v72, v73 quad_perm:[0,1,2,3] row_mask:0x1 bank_mask:0xf
	v_add_f32_dpp v108, v76, v77 quad_perm:[0,1,2,3] row_mask:0x2 bank_mask:0xf
	v_add_f32_dpp v108, v80, v81 quad_perm:[0,1,2,3] row_mask:0x4 bank_mask:0xf
	v_add_f32_dpp v108, v84, v85 quad_perm:[0,1,2,3] row_mask:0x8 bank_mask:0xf
	v_rcp_f32_e32 v109, v108
	s_mov_b32 s34, 0x3d0df4e0
	s_mov_b32 s35, s34
	v_mul_f32_e32 v118, v117, v109
	ds_read_b64 v[0:1], v67 offset:10240
	ds_read_b64 v[2:3], v65 offset:10264
	ds_read_b64 v[4:5], v67 offset:10304
	ds_read_b64 v[6:7], v65 offset:10328
	ds_read_b64 v[8:9], v67 offset:12424
	ds_read_b64 v[10:11], v67 offset:12416
	ds_read_b64 v[12:13], v67 offset:12488
	ds_read_b64 v[14:15], v67 offset:12480
	ds_read_b64 v[16:17], v65 offset:14608
	ds_read_b64 v[18:19], v67 offset:14600
	ds_read_b64 v[20:21], v65 offset:14672
	ds_read_b64 v[22:23], v67 offset:14664
	ds_read_b64 v[24:25], v65 offset:16792
	ds_read_b64 v[26:27], v65 offset:16784
	ds_read_b64 v[28:29], v65 offset:16856
	ds_read_b64 v[30:31], v65 offset:16848
	s_waitcnt lgkmcnt(0)
	v_mov_b64_e32 v[88:89], s[32:33]
	v_mov_b64_e32 v[92:93], s[32:33]
	v_mov_b64_e32 v[96:97], s[32:33]
	v_mov_b64_e32 v[104:105], s[32:33]
	s_nop 1
	v_smfmac_f32_16x16x64_bf16 v[88:91], v[68:71], v[0:7], v64
	v_smfmac_f32_16x16x64_bf16 v[92:95], v[68:71], v[8:15], v64
	v_smfmac_f32_16x16x64_bf16 v[96:99], v[68:71], v[16:23], v64
	v_smfmac_f32_16x16x64_bf16 v[104:107], v[68:71], v[24:31], v64
	s_nop 4
	v_add_f32_dpp v108, v88, v89 quad_perm:[0,1,2,3] row_mask:0x1 bank_mask:0xf
	v_add_f32_dpp v108, v92, v93 quad_perm:[0,1,2,3] row_mask:0x2 bank_mask:0xf
	v_add_f32_dpp v108, v96, v97 quad_perm:[0,1,2,3] row_mask:0x4 bank_mask:0xf
	v_add_f32_dpp v108, v104, v105 quad_perm:[0,1,2,3] row_mask:0x8 bank_mask:0xf
	v_add_f32_e32 v108, 0xab8cbccc, v108
	v_mul_f32_e32 v108, v118, v108
	s_nop 1
	v_add_f32_dpp v108, v108, v108 row_ror:8 row_mask:0xf bank_mask:0xf
	s_nop 1
	v_add_f32_dpp v108, v108, v108 row_ror:4 row_mask:0xf bank_mask:0xf
	s_nop 1
	v_add_f32_dpp v108, v108, v108 row_ror:2 row_mask:0xf bank_mask:0xf
	s_nop 1
	v_add_f32_dpp v108, v108, v108 row_ror:1 row_mask:0xf bank_mask:0xf
	s_nop 1
	v_mov_b32_e32 v109, v108
	s_nop 1
	v_permlane16_swap_b32_e32 v108, v109
	v_add_f32_e32 v108, v108, v109
	v_mov_b32_e32 v109, v108
	s_nop 1
	v_permlane32_swap_b32_e32 v108, v109
	v_add_f32_e32 v108, v108, v109
	v_cmp_eq_u32_e32 vcc, 0, v100
	s_and_saveexec_b64 s[0:1], vcc
	s_cbranch_execz .LBB1_38
	s_mul_i32 s0, s22, 5
	s_add_i32 s0, s0, s23
	s_mov_b32 s1, 0
	s_lshl_b64 s[0:1], s[0:1], 2
	s_add_u32 s0, s12, s0
	s_addc_u32 s1, s13, s1
	v_mov_b32_e32 v109, 0
	global_store_dword v109, v108, s[0:1]
